# gate/up and down phases: tile count and tile-table rows requested together, one combined wait on every path
# speedup vs baseline: 1.0117x; 1.0020x over previous
.LBB0_904:
	s_cmp_gt_i32 s6, 9
	s_cselect_b64 s[0:1], -1, 0
	s_cmp_lt_i32 s7, 10
	s_cselect_b64 s[2:3], -1, 0
	s_or_b64 s[0:1], s[0:1], s[2:3]
	s_and_b64 vcc, exec, s[0:1]
	s_cbranch_vccnz .LBB0_1038
	s_mov_b32 s98, s88
	s_and_b32 s99, s88, 31
	s_lshl_b32 s99, s99, 3
	s_lshr_b32 s88, s88, 5
	s_or_b32 s88, s88, s99
	s_waitcnt vmcnt(0)
	v_mov_b32_e32 v1, 0x420000
	v_mbcnt_lo_u32_b32 v0, -1, 0
	v_mbcnt_hi_u32_b32 v0, -1, v0
	global_load_dword v1, v1, s[94:95]
	s_and_b32 s0, s89, 0xffffffc0
	s_movk_i32 s1, 0x140
	v_add_u32_e32 v0, s0, v0
	s_add_u32 s2, s94, 0x420000
	s_addc_u32 s3, s95, 0
	v_cmp_gt_i32_e32 vcc, s1, v0
	v_mov_b32_e32 v2, v0
	v_ashrrev_i32_e32 v3, 31, v0
	v_lshl_add_u64 v[2:3], v[2:3], 2, s[2:3]
	global_load_dword v4, v[2:3], off offset:4
	s_waitcnt vmcnt(0)
	v_readfirstlane_b32 s41, v1
	s_and_saveexec_b64 s[0:1], vcc
	s_cbranch_execz .LBB0_907
	v_lshl_add_u32 v2, v0, 2, 0
	v_add_u32_e32 v2, 0x22400, v2
	s_waitcnt vmcnt(0)
	ds_write_b32 v2, v4

.LBB0_1038:
	s_cmp_gt_i32 s6, 10
	s_cselect_b64 s[0:1], -1, 0
	s_cmp_lt_i32 s7, 11
	s_cselect_b64 s[2:3], -1, 0
	s_or_b64 s[0:1], s[0:1], s[2:3]
	s_and_b64 vcc, exec, s[0:1]
	s_cbranch_vccnz .LBB0_1136
	s_mov_b32 s98, s88
	s_and_b32 s99, s88, 31
	s_lshl_b32 s99, s99, 3
	s_lshr_b32 s88, s88, 5
	s_or_b32 s88, s88, s99
	s_waitcnt vmcnt(0)
	v_mov_b32_e32 v1, 0x420000
	v_mbcnt_lo_u32_b32 v0, -1, 0
	v_mbcnt_hi_u32_b32 v0, -1, v0
	global_load_dword v1, v1, s[94:95]
	s_and_b32 s0, s89, 0xffffffc0
	s_movk_i32 s1, 0x140
	v_add_u32_e32 v0, s0, v0
	s_add_u32 s2, s94, 0x420000
	s_addc_u32 s3, s95, 0
	v_cmp_gt_i32_e32 vcc, s1, v0
	v_mov_b32_e32 v2, v0
	v_ashrrev_i32_e32 v3, 31, v0
	v_lshl_add_u64 v[2:3], v[2:3], 2, s[2:3]
	global_load_dword v4, v[2:3], off offset:4
	s_waitcnt vmcnt(0)
	v_readfirstlane_b32 s44, v1
	s_and_saveexec_b64 s[0:1], vcc
	s_cbranch_execz .LBB0_1041
	v_lshl_add_u32 v0, v0, 2, 0
	v_add_u32_e32 v0, 0x22400, v0
	s_waitcnt vmcnt(0)
	ds_write_b32 v0, v4

.LBB0_1727:
	s_cmp_gt_i32 s6, 25
	s_cselect_b64 s[0:1], -1, 0
	s_cmp_lt_i32 s7, 26
	s_cselect_b64 s[2:3], -1, 0
	s_or_b64 s[0:1], s[0:1], s[2:3]
	s_and_b64 vcc, exec, s[0:1]
	s_cbranch_vccnz .LBB0_1861
	s_mov_b32 s98, s88
	s_and_b32 s99, s88, 31
	s_lshl_b32 s99, s99, 3
	s_lshr_b32 s88, s88, 5
	s_or_b32 s88, s88, s99
	s_waitcnt vmcnt(0)
	v_mov_b32_e32 v1, 0x420000
	v_mbcnt_lo_u32_b32 v0, -1, 0
	v_mbcnt_hi_u32_b32 v0, -1, v0
	global_load_dword v1, v1, s[94:95]
	s_and_b32 s0, s89, 0xffffffc0
	s_movk_i32 s1, 0x140
	v_add_u32_e32 v0, s0, v0
	s_add_u32 s2, s94, 0x420000
	s_addc_u32 s3, s95, 0
	v_cmp_gt_i32_e32 vcc, s1, v0
	v_mov_b32_e32 v2, v0
	v_ashrrev_i32_e32 v3, 31, v0
	v_lshl_add_u64 v[2:3], v[2:3], 2, s[2:3]
	global_load_dword v4, v[2:3], off offset:4
	s_waitcnt vmcnt(0)
	v_readfirstlane_b32 s41, v1
	s_and_saveexec_b64 s[0:1], vcc
	s_cbranch_execz .LBB0_1730
	v_lshl_add_u32 v2, v0, 2, 0
	v_add_u32_e32 v2, 0x22400, v2
	s_waitcnt vmcnt(0)
	ds_write_b32 v2, v4

.LBB0_1861:
	s_cmp_gt_i32 s6, 26
	s_cselect_b64 s[0:1], -1, 0
	s_cmp_lt_i32 s7, 27
	s_cselect_b64 s[2:3], -1, 0
	s_or_b64 s[0:1], s[0:1], s[2:3]
	s_and_b64 vcc, exec, s[0:1]
	s_cbranch_vccnz .LBB0_1959
	s_mov_b32 s98, s88
	s_and_b32 s99, s88, 31
	s_lshl_b32 s99, s99, 3
	s_lshr_b32 s88, s88, 5
	s_or_b32 s88, s88, s99
	s_waitcnt vmcnt(0)
	v_mov_b32_e32 v1, 0x420000
	v_mbcnt_lo_u32_b32 v0, -1, 0
	v_mbcnt_hi_u32_b32 v0, -1, v0
	global_load_dword v1, v1, s[94:95]
	s_and_b32 s0, s89, 0xffffffc0
	s_movk_i32 s1, 0x140
	v_add_u32_e32 v0, s0, v0
	s_add_u32 s2, s94, 0x420000
	s_addc_u32 s3, s95, 0
	v_cmp_gt_i32_e32 vcc, s1, v0
	v_mov_b32_e32 v2, v0
	v_ashrrev_i32_e32 v3, 31, v0
	v_lshl_add_u64 v[2:3], v[2:3], 2, s[2:3]
	global_load_dword v4, v[2:3], off offset:4
	s_waitcnt vmcnt(0)
	v_readfirstlane_b32 s44, v1
	s_and_saveexec_b64 s[0:1], vcc
	s_cbranch_execz .LBB0_1864
	v_lshl_add_u32 v0, v0, 2, 0
	v_add_u32_e32 v0, 0x22400, v0
	s_waitcnt vmcnt(0)
	ds_write_b32 v0, v4

.LBB0_2635:
	s_cmp_gt_i32 s6, 41
	s_cselect_b64 s[0:1], -1, 0
	s_cmp_lt_i32 s7, 42
	s_cselect_b64 s[2:3], -1, 0
	s_or_b64 s[0:1], s[0:1], s[2:3]
	s_and_b64 vcc, exec, s[0:1]
	s_cbranch_vccnz .LBB0_2769
	s_mov_b32 s98, s88
	s_and_b32 s99, s88, 31
	s_lshl_b32 s99, s99, 3
	s_lshr_b32 s88, s88, 5
	s_or_b32 s88, s88, s99
	s_waitcnt vmcnt(0)
	v_mov_b32_e32 v1, 0x420000
	v_mbcnt_lo_u32_b32 v0, -1, 0
	v_mbcnt_hi_u32_b32 v0, -1, v0
	global_load_dword v1, v1, s[94:95]
	s_and_b32 s0, s89, 0xffffffc0
	s_movk_i32 s1, 0x140
	v_add_u32_e32 v0, s0, v0
	s_add_u32 s2, s94, 0x420000
	s_addc_u32 s3, s95, 0
	v_cmp_gt_i32_e32 vcc, s1, v0
	v_mov_b32_e32 v2, v0
	v_ashrrev_i32_e32 v3, 31, v0
	v_lshl_add_u64 v[2:3], v[2:3], 2, s[2:3]
	global_load_dword v4, v[2:3], off offset:4
	s_waitcnt vmcnt(0)
	v_readfirstlane_b32 s41, v1
	s_and_saveexec_b64 s[0:1], vcc
	s_cbranch_execz .LBB0_2638
	v_lshl_add_u32 v2, v0, 2, 0
	v_add_u32_e32 v2, 0x22400, v2
	s_waitcnt vmcnt(0)
	ds_write_b32 v2, v4

.LBB0_2769:
	s_cmp_gt_i32 s6, 42
	s_cselect_b64 s[0:1], -1, 0
	s_cmp_lt_i32 s7, 43
	s_cselect_b64 s[2:3], -1, 0
	s_or_b64 s[0:1], s[0:1], s[2:3]
	s_and_b64 vcc, exec, s[0:1]
	s_cbranch_vccnz .LBB0_2867
	s_mov_b32 s98, s88
	s_and_b32 s99, s88, 31
	s_lshl_b32 s99, s99, 3
	s_lshr_b32 s88, s88, 5
	s_or_b32 s88, s88, s99
	s_waitcnt vmcnt(0)
	v_mov_b32_e32 v1, 0x420000
	v_mbcnt_lo_u32_b32 v0, -1, 0
	v_mbcnt_hi_u32_b32 v0, -1, v0
	global_load_dword v1, v1, s[94:95]
	s_and_b32 s0, s89, 0xffffffc0
	s_movk_i32 s1, 0x140
	v_add_u32_e32 v0, s0, v0
	s_add_u32 s2, s94, 0x420000
	s_addc_u32 s3, s95, 0
	v_cmp_gt_i32_e32 vcc, s1, v0
	v_mov_b32_e32 v2, v0
	v_ashrrev_i32_e32 v3, 31, v0
	v_lshl_add_u64 v[2:3], v[2:3], 2, s[2:3]
	global_load_dword v4, v[2:3], off offset:4
	s_waitcnt vmcnt(0)
	v_readfirstlane_b32 s44, v1
	s_and_saveexec_b64 s[0:1], vcc
	s_cbranch_execz .LBB0_2772
	v_lshl_add_u32 v0, v0, 2, 0
	v_add_u32_e32 v0, 0x22400, v0
	s_waitcnt vmcnt(0)
	ds_write_b32 v0, v4

.LBB0_3598:
	s_cmp_gt_i32 s6, 57
	s_cselect_b64 s[0:1], -1, 0
	s_cmp_lt_i32 s7, 58
	s_cselect_b64 s[2:3], -1, 0
	s_or_b64 s[0:1], s[0:1], s[2:3]
	s_and_b64 vcc, exec, s[0:1]
	s_cbranch_vccnz .LBB0_3713
	s_mov_b32 s98, s88
	s_and_b32 s99, s88, 31
	s_lshl_b32 s99, s99, 3
	s_lshr_b32 s88, s88, 5
	s_or_b32 s88, s88, s99
	s_waitcnt vmcnt(0)
	v_mov_b32_e32 v1, 0x420000
	v_mbcnt_lo_u32_b32 v0, -1, 0
	v_mbcnt_hi_u32_b32 v0, -1, v0
	global_load_dword v1, v1, s[94:95]
	s_and_b32 s0, s89, 0xffffffc0
	s_movk_i32 s1, 0x140
	v_add_u32_e32 v0, s0, v0
	s_add_u32 s2, s94, 0x420000
	s_addc_u32 s3, s95, 0
	v_cmp_gt_i32_e32 vcc, s1, v0
	v_mov_b32_e32 v2, v0
	v_ashrrev_i32_e32 v3, 31, v0
	v_lshl_add_u64 v[2:3], v[2:3], 2, s[2:3]
	global_load_dword v4, v[2:3], off offset:4
	s_waitcnt vmcnt(0)
	v_readfirstlane_b32 s17, v1
	s_and_saveexec_b64 s[0:1], vcc
	s_cbranch_execz .LBB0_3601
	v_lshl_add_u32 v2, v0, 2, 0
	v_add_u32_e32 v2, 0x22400, v2
	s_waitcnt vmcnt(0)
	ds_write_b32 v2, v4

.LBB0_3713:
	s_cmp_gt_i32 s6, 58
	s_cselect_b64 s[0:1], -1, 0
	s_cmp_lt_i32 s7, 59
	s_cselect_b64 s[2:3], -1, 0
	s_or_b64 s[0:1], s[0:1], s[2:3]
	s_and_b64 vcc, exec, s[0:1]
	s_cbranch_vccnz .LBB0_3792
	s_mov_b32 s98, s88
	s_and_b32 s99, s88, 31
	s_lshl_b32 s99, s99, 3
	s_lshr_b32 s88, s88, 5
	s_or_b32 s88, s88, s99
	s_waitcnt vmcnt(0)
	v_mov_b32_e32 v1, 0x420000
	v_mbcnt_lo_u32_b32 v0, -1, 0
	v_mbcnt_hi_u32_b32 v0, -1, v0
	global_load_dword v1, v1, s[94:95]
	s_and_b32 s0, s89, 0xffffffc0
	s_movk_i32 s1, 0x140
	v_add_u32_e32 v0, s0, v0
	s_add_u32 s2, s94, 0x420000
	s_addc_u32 s3, s95, 0
	v_cmp_gt_i32_e32 vcc, s1, v0
	v_mov_b32_e32 v2, v0
	v_ashrrev_i32_e32 v3, 31, v0
	v_lshl_add_u64 v[2:3], v[2:3], 2, s[2:3]
	global_load_dword v4, v[2:3], off offset:4
	s_waitcnt vmcnt(0)
	v_readfirstlane_b32 s9, v1
	s_and_saveexec_b64 s[0:1], vcc
	s_cbranch_execz .LBB0_3716
	v_lshl_add_u32 v0, v0, 2, 0
	v_add_u32_e32 v0, 0x22400, v0
	s_waitcnt vmcnt(0)
	ds_write_b32 v0, v4
